# same as previous plus static token stride derived from gridDim.x instead of a constant
# speedup vs baseline: 1.0139x; 1.0011x over previous
.LBB0_719:
	s_lshl_b32 s6, s33, 3
	s_add_i32 s6, s6, s88
	v_mov_b32_e32 v247, s6
	s_ashr_i32 s89, s88, 31
	s_lshl_b64 s[74:75], s[88:89], 11
	s_lshl_b64 s[8:9], s[88:89], 2
	v_lshl_add_u64 v[24:25], v[128:129], 0, s[74:75]
	s_add_u32 s8, s37, s8
	global_load_dwordx4 v[20:23], v[24:25], off offset:1024
	s_addc_u32 s9, s73, s9
	global_load_dwordx4 v[24:27], v[24:25], off
	s_nop 0
	global_load_dword v248, v3, s[8:9]
	s_waitcnt vmcnt(6)
	v_lshlrev_b32_e32 v28, 16, v4
	v_cmp_lt_i32_e32 vcc, -1, v28
	v_lshlrev_b32_e32 v30, 16, v5
	v_lshlrev_b32_e32 v32, 16, v6
	v_cndmask_b32_e32 v29, v217, v218, vcc
	v_cmp_lt_i32_e32 vcc, -1, v4
	v_xor_b32_e32 v28, v29, v28
	v_lshlrev_b32_e32 v34, 16, v7
	v_cndmask_b32_e32 v29, v217, v218, vcc
	v_cmp_lt_i32_e32 vcc, -1, v30
	s_waitcnt vmcnt(3)
	v_lshlrev_b32_e32 v36, 16, v16
	v_lshlrev_b32_e32 v38, 16, v17
	v_cndmask_b32_e32 v31, v217, v218, vcc
	v_cmp_lt_i32_e32 vcc, -1, v5
	v_xor_b32_e32 v30, v31, v30
	v_lshlrev_b32_e32 v40, 16, v18
	v_cndmask_b32_e32 v31, v217, v218, vcc
	v_cmp_lt_i32_e32 vcc, -1, v32
	v_lshlrev_b32_e32 v42, 16, v19
	v_lshlrev_b32_e32 v44, 16, v12
	v_cndmask_b32_e32 v33, v217, v218, vcc
	v_cmp_lt_i32_e32 vcc, -1, v6
	v_xor_b32_e32 v32, v33, v32
	v_lshlrev_b32_e32 v46, 16, v13
	v_cndmask_b32_e32 v33, v217, v218, vcc
	v_cmp_lt_i32_e32 vcc, -1, v34
	v_lshlrev_b32_e32 v48, 16, v14
	v_lshlrev_b32_e32 v50, 16, v15
	v_cndmask_b32_e32 v35, v217, v218, vcc
	v_cmp_lt_i32_e32 vcc, -1, v7
	v_xor_b32_e32 v34, v35, v34
	v_lshlrev_b32_e32 v52, 16, v8
	v_cndmask_b32_e32 v35, v217, v218, vcc
	v_cmp_lt_i32_e32 vcc, -1, v36
	v_lshlrev_b32_e32 v54, 16, v9
	v_lshlrev_b32_e32 v56, 16, v10
	v_cndmask_b32_e32 v37, v217, v218, vcc
	v_cmp_lt_i32_e32 vcc, -1, v16
	v_xor_b32_e32 v36, v37, v36
	v_lshlrev_b32_e32 v58, 16, v11
	v_cndmask_b32_e32 v37, v217, v218, vcc
	v_cmp_lt_i32_e32 vcc, -1, v38
	v_bitop3_b32 v29, v29, v4, s90 bitop3:0x78
	v_bitop3_b32 v31, v31, v5, s90 bitop3:0x78
	v_cndmask_b32_e32 v39, v217, v218, vcc
	v_cmp_lt_i32_e32 vcc, -1, v17
	v_xor_b32_e32 v38, v39, v38
	v_bitop3_b32 v33, v33, v6, s90 bitop3:0x78
	v_cndmask_b32_e32 v39, v217, v218, vcc
	v_cmp_lt_i32_e32 vcc, -1, v40
	v_bitop3_b32 v35, v35, v7, s90 bitop3:0x78
	v_bitop3_b32 v37, v37, v16, s90 bitop3:0x78
	v_cndmask_b32_e32 v41, v217, v218, vcc
	v_cmp_lt_i32_e32 vcc, -1, v18
	v_xor_b32_e32 v40, v41, v40
	v_bitop3_b32 v39, v39, v17, s90 bitop3:0x78
	v_cndmask_b32_e32 v41, v217, v218, vcc
	v_cmp_lt_i32_e32 vcc, -1, v42
	v_bitop3_b32 v41, v41, v18, s90 bitop3:0x78
	v_sub_u32_e32 v28, v28, v201
	v_cndmask_b32_e32 v43, v217, v218, vcc
	v_cmp_lt_i32_e32 vcc, -1, v19
	v_xor_b32_e32 v42, v43, v42
	v_sub_u32_e32 v29, v29, v201
	v_cndmask_b32_e32 v43, v217, v218, vcc
	v_cmp_lt_i32_e32 vcc, -1, v44
	v_bitop3_b32 v43, v43, v19, s90 bitop3:0x78
	v_sub_u32_e32 v30, v30, v202
	v_cndmask_b32_e32 v45, v217, v218, vcc
	v_cmp_lt_i32_e32 vcc, -1, v12
	v_xor_b32_e32 v44, v45, v44
	v_sub_u32_e32 v31, v31, v202
	v_cndmask_b32_e32 v45, v217, v218, vcc
	v_cmp_lt_i32_e32 vcc, -1, v46
	v_bitop3_b32 v45, v45, v12, s90 bitop3:0x78
	v_sub_u32_e32 v32, v32, v203
	v_cndmask_b32_e32 v47, v217, v218, vcc
	v_cmp_lt_i32_e32 vcc, -1, v13
	v_xor_b32_e32 v46, v47, v46
	v_sub_u32_e32 v33, v33, v203
	v_cndmask_b32_e32 v47, v217, v218, vcc
	v_cmp_lt_i32_e32 vcc, -1, v48
	v_bitop3_b32 v47, v47, v13, s90 bitop3:0x78
	v_sub_u32_e32 v34, v34, v204
	v_cndmask_b32_e32 v49, v217, v218, vcc
	v_cmp_lt_i32_e32 vcc, -1, v14
	v_xor_b32_e32 v48, v49, v48
	v_sub_u32_e32 v35, v35, v204
	v_cndmask_b32_e32 v49, v217, v218, vcc
	v_cmp_lt_i32_e32 vcc, -1, v50
	v_bitop3_b32 v49, v49, v14, s90 bitop3:0x78
	v_sub_u32_e32 v36, v36, v205
	v_cndmask_b32_e32 v51, v217, v218, vcc
	v_cmp_lt_i32_e32 vcc, -1, v15
	v_xor_b32_e32 v50, v51, v50
	v_sub_u32_e32 v37, v37, v205
	v_cndmask_b32_e32 v51, v217, v218, vcc
	v_cmp_lt_i32_e32 vcc, -1, v52
	v_bitop3_b32 v51, v51, v15, s90 bitop3:0x78
	v_sub_u32_e32 v38, v38, v220
	v_cndmask_b32_e32 v53, v217, v218, vcc
	v_cmp_lt_i32_e32 vcc, -1, v8
	v_xor_b32_e32 v52, v53, v52
	v_sub_u32_e32 v39, v39, v220
	v_cndmask_b32_e32 v53, v217, v218, vcc
	v_cmp_lt_i32_e32 vcc, -1, v54
	v_bitop3_b32 v53, v53, v8, s90 bitop3:0x78
	v_sub_u32_e32 v40, v40, v221
	v_cndmask_b32_e32 v55, v217, v218, vcc
	v_cmp_lt_i32_e32 vcc, -1, v9
	v_xor_b32_e32 v54, v55, v54
	v_sub_u32_e32 v41, v41, v221
	v_cndmask_b32_e32 v55, v217, v218, vcc
	v_cmp_lt_i32_e32 vcc, -1, v56
	v_bitop3_b32 v55, v55, v9, s90 bitop3:0x78
	v_sub_u32_e32 v42, v42, v222
	v_cndmask_b32_e32 v57, v217, v218, vcc
	v_cmp_lt_i32_e32 vcc, -1, v10
	v_xor_b32_e32 v56, v57, v56
	v_sub_u32_e32 v43, v43, v222
	v_cndmask_b32_e32 v57, v217, v218, vcc
	v_cmp_lt_i32_e32 vcc, -1, v58
	v_bitop3_b32 v57, v57, v10, s90 bitop3:0x78
	v_sub_u32_e32 v44, v44, v223
	v_cndmask_b32_e32 v59, v217, v218, vcc
	v_cmp_lt_i32_e32 vcc, -1, v11
	v_xor_b32_e32 v58, v59, v58
	v_sub_u32_e32 v45, v45, v223
	v_cndmask_b32_e32 v59, v217, v218, vcc
	v_bitop3_b32 v59, v59, v11, s90 bitop3:0x78
	v_sub_u32_e32 v46, v46, v224
	v_sub_u32_e32 v47, v47, v224
	v_sub_u32_e32 v48, v48, v225
	v_sub_u32_e32 v49, v49, v225
	v_sub_u32_e32 v50, v50, v226
	v_sub_u32_e32 v51, v51, v226
	v_sub_u32_e32 v52, v52, v227
	v_sub_u32_e32 v53, v53, v227
	v_sub_u32_e32 v54, v54, v228
	v_sub_u32_e32 v55, v55, v228
	v_sub_u32_e32 v56, v56, v229
	v_sub_u32_e32 v57, v57, v229
	v_sub_u32_e32 v58, v58, v230
	v_sub_u32_e32 v59, v59, v230
	v_add_u32_e32 v28, 0x7f, v28
	v_add_u32_e32 v29, 0x7e, v29
	v_add_u32_e32 v30, 0x7f, v30
	v_add_u32_e32 v31, 0x7e, v31
	v_add_u32_e32 v32, 0x7f, v32
	v_add_u32_e32 v33, 0x7e, v33
	v_add_u32_e32 v34, 0x7f, v34
	v_add_u32_e32 v35, 0x7e, v35
	v_add_u32_e32 v36, 0x7f, v36
	v_add_u32_e32 v37, 0x7e, v37
	v_add_u32_e32 v38, 0x7f, v38
	v_add_u32_e32 v39, 0x7e, v39
	v_add_u32_e32 v40, 0x7f, v40
	v_add_u32_e32 v41, 0x7e, v41
	v_add_u32_e32 v42, 0x7f, v42
	v_add_u32_e32 v43, 0x7e, v43
	v_add_u32_e32 v44, 0x7f, v44
	v_add_u32_e32 v45, 0x7e, v45
	v_add_u32_e32 v46, 0x7f, v46
	v_add_u32_e32 v47, 0x7e, v47
	v_add_u32_e32 v48, 0x7f, v48
	v_add_u32_e32 v49, 0x7e, v49
	v_add_u32_e32 v50, 0x7f, v50
	v_add_u32_e32 v51, 0x7e, v51
	v_add_u32_e32 v52, 0x7f, v52
	v_add_u32_e32 v53, 0x7e, v53
	v_add_u32_e32 v54, 0x7f, v54
	v_add_u32_e32 v55, 0x7e, v55
	v_add_u32_e32 v56, 0x7f, v56
	v_add_u32_e32 v57, 0x7e, v57
	v_add_u32_e32 v58, 0x7f, v58
	v_add_u32_e32 v59, 0x7e, v59
	v_max_u32_e32 v60, v28, v29
	v_min_u32_e32 v28, v28, v29
	v_max_u32_e32 v29, v30, v31
	v_min_u32_e32 v30, v30, v31
	v_max_u32_e32 v31, v32, v33
	v_min_u32_e32 v32, v32, v33
	v_max_u32_e32 v33, v34, v35
	v_min_u32_e32 v34, v34, v35
	v_max_u32_e32 v35, v36, v37
	v_min_u32_e32 v36, v36, v37
	v_max_u32_e32 v37, v38, v39
	v_min_u32_e32 v38, v38, v39
	v_max_u32_e32 v39, v40, v41
	v_min_u32_e32 v40, v40, v41
	v_max_u32_e32 v41, v42, v43
	v_min_u32_e32 v42, v42, v43
	v_max_u32_e32 v43, v44, v45
	v_min_u32_e32 v44, v44, v45
	v_max_u32_e32 v45, v46, v47
	v_min_u32_e32 v46, v46, v47
	v_max_u32_e32 v47, v48, v49
	v_min_u32_e32 v48, v48, v49
	v_max_u32_e32 v49, v50, v51
	v_min_u32_e32 v50, v50, v51
	v_max_u32_e32 v51, v52, v53
	v_min_u32_e32 v52, v52, v53
	v_max_u32_e32 v53, v54, v55
	v_min_u32_e32 v54, v54, v55
	v_max_u32_e32 v55, v56, v57
	v_min_u32_e32 v56, v56, v57
	v_max_u32_e32 v57, v58, v59
	v_min_u32_e32 v58, v58, v59
	v_max_u32_e32 v59, v60, v30
	v_min_u32_e32 v30, v60, v30
	v_max_u32_e32 v60, v28, v29
	v_min_u32_e32 v28, v28, v29
	v_max_u32_e32 v29, v31, v34
	v_min_u32_e32 v31, v31, v34
	v_max_u32_e32 v34, v32, v33
	v_min_u32_e32 v32, v32, v33
	v_max_u32_e32 v33, v35, v38
	v_min_u32_e32 v35, v35, v38
	v_max_u32_e32 v38, v36, v37
	v_min_u32_e32 v36, v36, v37
	v_max_u32_e32 v37, v39, v42
	v_min_u32_e32 v39, v39, v42
	v_max_u32_e32 v42, v40, v41
	v_min_u32_e32 v40, v40, v41
	v_max_u32_e32 v41, v43, v46
	v_min_u32_e32 v43, v43, v46
	v_max_u32_e32 v46, v44, v45
	v_min_u32_e32 v44, v44, v45
	v_max_u32_e32 v45, v47, v50
	v_min_u32_e32 v47, v47, v50
	v_max_u32_e32 v50, v48, v49
	v_min_u32_e32 v48, v48, v49
	v_max_u32_e32 v49, v51, v54
	v_min_u32_e32 v51, v51, v54
	v_max_u32_e32 v54, v52, v53
	v_min_u32_e32 v52, v52, v53
	v_max_u32_e32 v53, v55, v58
	v_min_u32_e32 v55, v55, v58
	v_max_u32_e32 v58, v56, v57
	v_min_u32_e32 v56, v56, v57
	v_max_u32_e32 v57, v59, v60
	v_min_u32_e32 v59, v59, v60
	v_max_u32_e32 v60, v30, v28
	v_min_u32_e32 v28, v30, v28
	v_max_u32_e32 v30, v31, v32
	v_min_u32_e32 v31, v31, v32
	v_max_u32_e32 v32, v29, v34
	v_min_u32_e32 v29, v29, v34
	v_max_u32_e32 v34, v33, v38
	v_min_u32_e32 v33, v33, v38
	v_max_u32_e32 v38, v35, v36
	v_min_u32_e32 v35, v35, v36
	v_max_u32_e32 v36, v39, v40
	v_min_u32_e32 v39, v39, v40
	v_max_u32_e32 v40, v37, v42
	v_min_u32_e32 v37, v37, v42
	v_max_u32_e32 v42, v41, v46
	v_min_u32_e32 v41, v41, v46
	v_max_u32_e32 v46, v43, v44
	v_min_u32_e32 v43, v43, v44
	v_max_u32_e32 v44, v47, v48
	v_min_u32_e32 v47, v47, v48
	v_max_u32_e32 v48, v45, v50
	v_min_u32_e32 v45, v45, v50
	v_max_u32_e32 v50, v49, v54
	v_min_u32_e32 v49, v49, v54
	v_max_u32_e32 v54, v51, v52
	v_min_u32_e32 v51, v51, v52
	v_max_u32_e32 v52, v55, v56
	v_min_u32_e32 v55, v55, v56
	v_max_u32_e32 v56, v53, v58
	v_min_u32_e32 v53, v53, v58
	v_max_u32_e32 v58, v57, v31
	v_min_u32_e32 v31, v57, v31
	v_max_u32_e32 v57, v59, v30
	v_min_u32_e32 v30, v59, v30
	v_max_u32_e32 v59, v60, v29
	v_min_u32_e32 v29, v60, v29
	v_max_u32_e32 v60, v28, v32
	v_min_u32_e32 v28, v28, v32
	v_max_u32_e32 v32, v34, v39
	v_min_u32_e32 v34, v34, v39
	v_max_u32_e32 v39, v33, v36
	v_min_u32_e32 v33, v33, v36
	v_max_u32_e32 v36, v38, v37
	v_min_u32_e32 v37, v38, v37
	v_max_u32_e32 v38, v35, v40
	v_min_u32_e32 v35, v35, v40
	v_max_u32_e32 v40, v42, v47
	v_min_u32_e32 v42, v42, v47
	v_max_u32_e32 v47, v41, v44
	v_min_u32_e32 v41, v41, v44
	v_max_u32_e32 v44, v46, v45
	v_min_u32_e32 v45, v46, v45
	v_max_u32_e32 v46, v43, v48
	v_min_u32_e32 v43, v43, v48
	v_max_u32_e32 v48, v50, v55
	v_min_u32_e32 v50, v50, v55
	v_max_u32_e32 v55, v49, v52
	v_min_u32_e32 v49, v49, v52
	v_max_u32_e32 v52, v54, v53
	v_min_u32_e32 v53, v54, v53
	v_max_u32_e32 v54, v51, v56
	v_min_u32_e32 v51, v51, v56
	v_max_u32_e32 v56, v58, v59
	v_min_u32_e32 v58, v58, v59
	v_max_u32_e32 v59, v57, v60
	v_min_u32_e32 v57, v57, v60
	v_max_u32_e32 v60, v31, v29
	v_min_u32_e32 v29, v31, v29
	v_max_u32_e32 v31, v30, v28
	v_min_u32_e32 v28, v30, v28
	v_max_u32_e32 v30, v34, v37
	v_min_u32_e32 v34, v34, v37
	v_max_u32_e32 v37, v33, v35
	v_min_u32_e32 v33, v33, v35
	v_max_u32_e32 v35, v32, v36
	v_min_u32_e32 v32, v32, v36
	v_max_u32_e32 v36, v39, v38
	v_min_u32_e32 v38, v39, v38
	v_max_u32_e32 v39, v40, v44
	v_min_u32_e32 v40, v40, v44
	v_max_u32_e32 v44, v47, v46
	v_min_u32_e32 v46, v47, v46
	v_max_u32_e32 v47, v42, v45
	v_min_u32_e32 v42, v42, v45
	v_max_u32_e32 v45, v41, v43
	v_min_u32_e32 v41, v41, v43
	v_max_u32_e32 v43, v50, v53
	v_min_u32_e32 v50, v50, v53
	v_max_u32_e32 v53, v49, v51
	v_min_u32_e32 v49, v49, v51
	v_max_u32_e32 v51, v48, v52
	v_min_u32_e32 v48, v48, v52
	v_max_u32_e32 v52, v55, v54
	v_min_u32_e32 v54, v55, v54
	v_max_u32_e32 v55, v56, v59
	v_min_u32_e32 v56, v56, v59
	v_max_u32_e32 v59, v58, v57
	v_min_u32_e32 v57, v58, v57
	v_max_u32_e32 v58, v60, v31
	v_min_u32_e32 v31, v60, v31
	v_max_u32_e32 v60, v29, v28
	v_min_u32_e32 v28, v29, v28
	v_max_u32_e32 v29, v34, v33
	v_min_u32_e32 v33, v34, v33
	v_max_u32_e32 v34, v30, v37
	v_min_u32_e32 v30, v30, v37
	v_max_u32_e32 v37, v32, v38
	v_min_u32_e32 v32, v32, v38
	v_max_u32_e32 v38, v35, v36
	v_min_u32_e32 v35, v35, v36
	v_max_u32_e32 v36, v39, v44
	v_min_u32_e32 v39, v39, v44
	v_max_u32_e32 v44, v40, v46
	v_min_u32_e32 v40, v40, v46
	v_max_u32_e32 v46, v47, v45
	v_min_u32_e32 v45, v47, v45
	v_max_u32_e32 v47, v42, v41
	v_min_u32_e32 v41, v42, v41
	v_max_u32_e32 v42, v50, v49
	v_min_u32_e32 v49, v50, v49
	v_max_u32_e32 v50, v43, v53
	v_min_u32_e32 v43, v43, v53
	v_max_u32_e32 v53, v48, v54
	v_min_u32_e32 v48, v48, v54
	v_max_u32_e32 v54, v51, v52
	v_min_u32_e32 v51, v51, v52
	v_max_u32_e32 v52, v55, v33
	v_min_u32_e32 v33, v55, v33
	v_max_u32_e32 v55, v56, v29
	v_min_u32_e32 v29, v56, v29
	v_max_u32_e32 v56, v59, v30
	v_min_u32_e32 v30, v59, v30
	v_max_u32_e32 v59, v57, v34
	v_min_u32_e32 v34, v57, v34
	v_max_u32_e32 v57, v58, v32
	v_min_u32_e32 v32, v58, v32
	v_max_u32_e32 v58, v31, v37
	v_min_u32_e32 v31, v31, v37
	v_max_u32_e32 v37, v60, v35
	v_min_u32_e32 v35, v60, v35
	v_max_u32_e32 v60, v28, v38
	v_min_u32_e32 v28, v28, v38
	v_max_u32_e32 v38, v36, v49
	v_min_u32_e32 v36, v36, v49
	v_max_u32_e32 v49, v39, v42
	v_min_u32_e32 v39, v39, v42
	v_max_u32_e32 v42, v44, v43
	v_min_u32_e32 v43, v44, v43
	v_max_u32_e32 v44, v40, v50
	v_min_u32_e32 v40, v40, v50
	v_max_u32_e32 v50, v46, v48
	v_min_u32_e32 v46, v46, v48
	v_max_u32_e32 v48, v45, v53
	v_min_u32_e32 v45, v45, v53
	v_max_u32_e32 v53, v47, v51
	v_min_u32_e32 v47, v47, v51
	v_max_u32_e32 v51, v41, v54
	v_min_u32_e32 v41, v41, v54
	v_max_u32_e32 v54, v52, v57
	v_min_u32_e32 v52, v52, v57
	v_max_u32_e32 v57, v55, v58
	v_min_u32_e32 v55, v55, v58
	v_max_u32_e32 v58, v56, v37
	v_min_u32_e32 v37, v56, v37
	v_max_u32_e32 v56, v59, v60
	v_min_u32_e32 v59, v59, v60
	v_max_u32_e32 v60, v33, v32
	v_min_u32_e32 v32, v33, v32
	v_max_u32_e32 v33, v29, v31
	v_min_u32_e32 v29, v29, v31
	v_max_u32_e32 v31, v30, v35
	v_min_u32_e32 v30, v30, v35
	v_max_u32_e32 v35, v34, v28
	v_min_u32_e32 v28, v34, v28
	v_max_u32_e32 v34, v36, v46
	v_min_u32_e32 v36, v36, v46
	v_max_u32_e32 v46, v39, v45
	v_min_u32_e32 v39, v39, v45
	v_max_u32_e32 v45, v43, v47
	v_min_u32_e32 v43, v43, v47
	v_max_u32_e32 v47, v40, v41
	v_min_u32_e32 v40, v40, v41
	v_max_u32_e32 v41, v38, v50
	v_min_u32_e32 v38, v38, v50
	v_max_u32_e32 v50, v49, v48
	v_min_u32_e32 v48, v49, v48
	v_max_u32_e32 v49, v42, v53
	v_min_u32_e32 v42, v42, v53
	v_max_u32_e32 v53, v44, v51
	v_min_u32_e32 v44, v44, v51
	v_max_u32_e32 v51, v54, v58
	v_min_u32_e32 v54, v54, v58
	v_max_u32_e32 v58, v57, v56
	v_min_u32_e32 v56, v57, v56
	v_max_u32_e32 v57, v52, v37
	v_min_u32_e32 v37, v52, v37
	v_max_u32_e32 v52, v55, v59
	v_min_u32_e32 v55, v55, v59
	v_max_u32_e32 v59, v60, v31
	v_min_u32_e32 v31, v60, v31
	v_max_u32_e32 v60, v33, v35
	v_min_u32_e32 v33, v33, v35
	v_max_u32_e32 v35, v32, v30
	v_min_u32_e32 v30, v32, v30
	v_max_u32_e32 v32, v29, v28
	v_min_u32_e32 v28, v29, v28
	v_max_u32_e32 v29, v36, v43
	v_min_u32_e32 v36, v36, v43
	v_max_u32_e32 v43, v39, v40
	v_min_u32_e32 v39, v39, v40
	v_max_u32_e32 v40, v34, v45
	v_min_u32_e32 v34, v34, v45
	v_max_u32_e32 v45, v46, v47
	v_min_u32_e32 v46, v46, v47
	v_max_u32_e32 v47, v38, v42
	v_min_u32_e32 v38, v38, v42
	v_max_u32_e32 v42, v48, v44
	v_min_u32_e32 v44, v48, v44
	v_max_u32_e32 v48, v41, v49
	v_min_u32_e32 v41, v41, v49
	v_max_u32_e32 v49, v50, v53
	v_min_u32_e32 v50, v50, v53
	v_min_u32_e32 v53, v51, v58
	v_min_u32_e32 v61, v54, v56
	v_min_u32_e32 v62, v57, v52
	v_min_u32_e32 v63, v37, v55
	v_min_u32_e32 v64, v59, v60
	v_min_u32_e32 v65, v31, v33
	v_min_u32_e32 v66, v35, v32
	v_min_u32_e32 v67, v30, v28
	v_min_u32_e32 v68, v36, v39
	v_min_u32_e32 v69, v29, v43
	v_min_u32_e32 v70, v34, v46
	v_min_u32_e32 v71, v40, v45
	v_min_u32_e32 v72, v38, v44
	v_min_u32_e32 v73, v47, v42
	v_min_u32_e32 v74, v41, v50
	v_min_u32_e32 v75, v48, v49
	v_max3_u32 v51, v51, v58, v68
	v_max3_u32 v36, v53, v36, v39
	v_max3_u32 v39, v54, v56, v69
	v_max3_u32 v29, v61, v29, v43
	v_max3_u32 v43, v57, v52, v70
	v_max3_u32 v34, v62, v34, v46
	v_max3_u32 v37, v37, v55, v71
	v_max3_u32 v40, v63, v40, v45
	v_max3_u32 v45, v59, v60, v72
	v_max3_u32 v38, v64, v38, v44
	v_max3_u32 v31, v31, v33, v73
	v_max3_u32 v33, v65, v47, v42
	v_max3_u32 v32, v35, v32, v74
	v_max3_u32 v35, v66, v41, v50
	v_max3_u32 v28, v30, v28, v75
	v_max3_u32 v30, v67, v48, v49
	v_max_u32_e32 v41, v51, v45
	v_min_u32_e32 v42, v51, v45
	v_max_u32_e32 v44, v36, v38
	v_min_u32_e32 v36, v36, v38
	v_max_u32_e32 v38, v39, v31
	v_min_u32_e32 v31, v39, v31
	v_max_u32_e32 v39, v29, v33
	v_min_u32_e32 v29, v29, v33
	v_max_u32_e32 v33, v43, v32
	v_min_u32_e32 v32, v43, v32
	v_max_u32_e32 v43, v34, v35
	v_min_u32_e32 v34, v34, v35
	v_max_u32_e32 v35, v37, v28
	v_min_u32_e32 v28, v37, v28
	v_max_u32_e32 v37, v40, v30
	v_min_u32_e32 v30, v40, v30
	v_max_u32_e32 v40, v41, v33
	v_min_u32_e32 v33, v41, v33
	v_max_u32_e32 v41, v44, v43
	v_min_u32_e32 v43, v44, v43
	v_max_u32_e32 v44, v38, v35
	v_min_u32_e32 v35, v38, v35
	v_max_u32_e32 v38, v39, v37
	v_min_u32_e32 v37, v39, v37
	v_max_u32_e32 v39, v42, v32
	v_min_u32_e32 v32, v42, v32
	v_max_u32_e32 v42, v36, v34
	v_min_u32_e32 v34, v36, v34
	v_max_u32_e32 v36, v31, v28
	v_min_u32_e32 v28, v31, v28
	v_max_u32_e32 v31, v29, v30
	v_min_u32_e32 v29, v29, v30
	v_max_u32_e32 v30, v40, v44
	v_min_u32_e32 v40, v40, v44
	v_max_u32_e32 v44, v41, v38
	v_min_u32_e32 v38, v41, v38
	v_max_u32_e32 v41, v33, v35
	v_min_u32_e32 v33, v33, v35
	v_max_u32_e32 v35, v43, v37
	v_min_u32_e32 v37, v43, v37
	v_max_u32_e32 v43, v39, v36
	v_min_u32_e32 v36, v39, v36
	v_max_u32_e32 v39, v42, v31
	v_min_u32_e32 v31, v42, v31
	v_max_u32_e32 v42, v32, v28
	v_min_u32_e32 v28, v32, v28
	v_max_u32_e32 v32, v34, v29
	v_min_u32_e32 v29, v34, v29
	v_max_u32_e32 v34, v30, v44
	v_min_u32_e32 v30, v30, v44
	v_max_u32_e32 v44, v40, v38
	v_min_u32_e32 v38, v40, v38
	v_max_u32_e32 v40, v41, v35
	v_min_u32_e32 v35, v41, v35
	v_max_u32_e32 v41, v33, v37
	v_min_u32_e32 v33, v33, v37
	v_max_u32_e32 v37, v43, v39
	v_min_u32_e32 v39, v43, v39
	v_max_u32_e32 v43, v36, v31
	v_min_u32_e32 v31, v36, v31
	v_max_u32_e32 v36, v42, v32
	v_min_u32_e32 v32, v42, v32
	v_max_u32_e32 v42, v28, v29
	v_min_u32_e32 v28, v28, v29
	v_max_u32_dpp v46, v32, v44 quad_perm:[1,0,3,2] row_mask:0xf bank_mask:0xf bound_ctrl:1
	v_max_u32_dpp v45, v42, v30 quad_perm:[1,0,3,2] row_mask:0xf bank_mask:0xf bound_ctrl:1
	v_max_u32_dpp v29, v28, v34 quad_perm:[1,0,3,2] row_mask:0xf bank_mask:0xf bound_ctrl:1
	v_max_u32_dpp v47, v36, v38 quad_perm:[1,0,3,2] row_mask:0xf bank_mask:0xf bound_ctrl:1
	v_max_u32_dpp v48, v31, v40 quad_perm:[1,0,3,2] row_mask:0xf bank_mask:0xf bound_ctrl:1
	v_max_u32_dpp v49, v43, v35 quad_perm:[1,0,3,2] row_mask:0xf bank_mask:0xf bound_ctrl:1
	v_max_u32_dpp v50, v39, v41 quad_perm:[1,0,3,2] row_mask:0xf bank_mask:0xf bound_ctrl:1
	v_max_u32_dpp v51, v37, v33 quad_perm:[1,0,3,2] row_mask:0xf bank_mask:0xf bound_ctrl:1
	v_max_u32_dpp v33, v33, v37 quad_perm:[1,0,3,2] row_mask:0xf bank_mask:0xf bound_ctrl:1
	v_max_u32_dpp v37, v41, v39 quad_perm:[1,0,3,2] row_mask:0xf bank_mask:0xf bound_ctrl:1
	v_max_u32_dpp v35, v35, v43 quad_perm:[1,0,3,2] row_mask:0xf bank_mask:0xf bound_ctrl:1
	v_max_u32_dpp v31, v40, v31 quad_perm:[1,0,3,2] row_mask:0xf bank_mask:0xf bound_ctrl:1
	v_max_u32_dpp v36, v38, v36 quad_perm:[1,0,3,2] row_mask:0xf bank_mask:0xf bound_ctrl:1
	v_max_u32_dpp v32, v44, v32 quad_perm:[1,0,3,2] row_mask:0xf bank_mask:0xf bound_ctrl:1
	v_max_u32_dpp v30, v30, v42 quad_perm:[1,0,3,2] row_mask:0xf bank_mask:0xf bound_ctrl:1
	v_max_u32_dpp v28, v34, v28 quad_perm:[1,0,3,2] row_mask:0xf bank_mask:0xf bound_ctrl:1
	v_max_u32_e32 v34, v29, v33
	v_min_u32_e32 v29, v29, v33
	v_max_u32_e32 v33, v45, v37
	v_min_u32_e32 v37, v45, v37
	v_max_u32_e32 v38, v46, v35
	v_min_u32_e32 v35, v46, v35
	v_max_u32_e32 v39, v47, v31
	v_min_u32_e32 v31, v47, v31
	v_max_u32_e32 v40, v48, v36
	v_min_u32_e32 v36, v48, v36
	v_max_u32_e32 v41, v49, v32
	v_min_u32_e32 v32, v49, v32
	v_max_u32_e32 v42, v50, v30
	v_min_u32_e32 v30, v50, v30
	v_max_u32_e32 v43, v51, v28
	v_min_u32_e32 v28, v51, v28
	v_max_u32_e32 v44, v34, v40
	v_min_u32_e32 v34, v34, v40
	v_max_u32_e32 v40, v33, v41
	v_min_u32_e32 v33, v33, v41
	v_max_u32_e32 v41, v38, v42
	v_min_u32_e32 v38, v38, v42
	v_max_u32_e32 v42, v39, v43
	v_min_u32_e32 v39, v39, v43
	v_max_u32_e32 v43, v29, v36
	v_min_u32_e32 v29, v29, v36
	v_max_u32_e32 v36, v37, v32
	v_min_u32_e32 v32, v37, v32
	v_max_u32_e32 v37, v35, v30
	v_min_u32_e32 v30, v35, v30
	v_max_u32_e32 v35, v31, v28
	v_min_u32_e32 v28, v31, v28
	v_max_u32_e32 v31, v44, v41
	v_min_u32_e32 v41, v44, v41
	v_max_u32_e32 v44, v40, v42
	v_min_u32_e32 v42, v40, v42
	v_max_u32_e32 v45, v34, v38
	v_min_u32_e32 v34, v34, v38
	v_max_u32_e32 v38, v33, v39
	v_min_u32_e32 v33, v33, v39
	v_max_u32_e32 v39, v43, v37
	v_min_u32_e32 v43, v43, v37
	v_max_u32_e32 v46, v36, v35
	v_min_u32_e32 v35, v36, v35
	v_max_u32_e32 v47, v29, v30
	v_min_u32_e32 v50, v29, v30
	v_max_u32_e32 v51, v32, v28
	v_min_u32_e32 v52, v32, v28
	v_max_u32_e32 v40, v31, v44
	v_min_u32_e32 v30, v31, v44
	v_max_u32_e32 v36, v41, v42
	v_min_u32_e32 v28, v41, v42
	v_max_u32_e32 v41, v45, v38
	v_min_u32_e32 v31, v45, v38
	v_max_u32_e32 v37, v34, v33
	v_min_u32_e32 v29, v34, v33
	v_max_u32_e32 v48, v39, v46
	v_min_u32_e32 v34, v39, v46
	v_max_u32_e32 v42, v43, v35
	v_min_u32_e32 v32, v43, v35
	v_max_u32_e32 v49, v47, v51
	v_min_u32_e32 v35, v47, v51
	v_max_u32_e32 v44, v50, v52
	v_min_u32_e32 v33, v50, v52
	v_mov_b32_dpp v52, v35 quad_perm:[2,3,0,1] row_mask:0xf bank_mask:0xf bound_ctrl:1
	v_mov_b32_dpp v43, v44 quad_perm:[2,3,0,1] row_mask:0xf bank_mask:0xf bound_ctrl:1
	v_mov_b32_dpp v54, v33 quad_perm:[2,3,0,1] row_mask:0xf bank_mask:0xf bound_ctrl:1
	v_mov_b32_dpp v38, v49 quad_perm:[2,3,0,1] row_mask:0xf bank_mask:0xf bound_ctrl:1
	v_mov_b32_dpp v55, v32 quad_perm:[2,3,0,1] row_mask:0xf bank_mask:0xf bound_ctrl:1
	v_mov_b32_dpp v45, v42 quad_perm:[2,3,0,1] row_mask:0xf bank_mask:0xf bound_ctrl:1
	v_mov_b32_dpp v53, v34 quad_perm:[2,3,0,1] row_mask:0xf bank_mask:0xf bound_ctrl:1
	v_mov_b32_dpp v39, v48 quad_perm:[2,3,0,1] row_mask:0xf bank_mask:0xf bound_ctrl:1
	v_mov_b32_dpp v58, v29 quad_perm:[2,3,0,1] row_mask:0xf bank_mask:0xf bound_ctrl:1
	v_mov_b32_dpp v50, v37 quad_perm:[2,3,0,1] row_mask:0xf bank_mask:0xf bound_ctrl:1
	v_mov_b32_dpp v56, v31 quad_perm:[2,3,0,1] row_mask:0xf bank_mask:0xf bound_ctrl:1
	v_mov_b32_dpp v46, v41 quad_perm:[2,3,0,1] row_mask:0xf bank_mask:0xf bound_ctrl:1
	v_mov_b32_dpp v59, v28 quad_perm:[2,3,0,1] row_mask:0xf bank_mask:0xf bound_ctrl:1
	v_mov_b32_dpp v51, v36 quad_perm:[2,3,0,1] row_mask:0xf bank_mask:0xf bound_ctrl:1
	v_mov_b32_dpp v57, v30 quad_perm:[2,3,0,1] row_mask:0xf bank_mask:0xf bound_ctrl:1
	v_mov_b32_dpp v47, v40 quad_perm:[2,3,0,1] row_mask:0xf bank_mask:0xf bound_ctrl:1
	s_and_saveexec_b64 s[8:9], s[46:47]
	s_cbranch_execz .LBB0_725
	v_max_u32_e32 v40, v40, v54
	v_max_u32_e32 v48, v48, v58
	v_max_u32_e32 v41, v41, v55
	v_max_u32_e32 v49, v49, v59
	v_max_u32_e32 v36, v36, v52
	v_max_u32_e32 v42, v42, v56
	v_max_u32_e32 v37, v37, v53
	v_max_u32_e32 v44, v44, v57
	v_max_u32_e32 v43, v30, v43
	v_max_u32_e32 v50, v34, v50
	v_max_u32_e32 v45, v31, v45
	v_max_u32_e32 v51, v35, v51
	v_max_u32_e32 v38, v28, v38
	v_max_u32_e32 v46, v32, v46
	v_max_u32_e32 v39, v29, v39
	v_max_u32_e32 v47, v33, v47
	v_min_u32_e32 v54, v40, v48
	v_min_u32_e32 v55, v41, v49
	v_min_u32_e32 v52, v36, v42
	v_min_u32_e32 v53, v37, v44
	v_min_u32_e32 v34, v43, v50
	v_min_u32_e32 v35, v45, v51
	v_min_u32_e32 v32, v38, v46
	v_min_u32_e32 v33, v39, v47
	v_max_u32_e32 v40, v40, v48
	v_max_u32_e32 v41, v41, v49
	v_max_u32_e32 v42, v36, v42
	v_max_u32_e32 v44, v37, v44
	v_max_u32_e32 v43, v43, v50
	v_max_u32_e32 v45, v45, v51
	v_max_u32_e32 v46, v38, v46
	v_max_u32_e32 v47, v39, v47
	v_min_u32_e32 v48, v40, v41
	v_min_u32_e32 v36, v42, v44
	v_min_u32_e32 v49, v43, v45
	v_max_u32_e32 v40, v40, v41
	v_max_u32_e32 v41, v42, v44
	v_max_u32_e32 v44, v43, v45
	v_max_u32_e32 v45, v46, v47
	v_min_u32_e32 v58, v54, v55
	v_min_u32_e32 v56, v52, v53
	v_min_u32_e32 v59, v34, v35
	v_min_u32_e32 v28, v32, v33
	v_max_u32_e32 v54, v54, v55
	v_max_u32_e32 v52, v52, v53
	v_max_u32_e32 v55, v34, v35
	v_max_u32_e32 v32, v32, v33
	v_min_u32_e32 v50, v46, v47
	v_min_u32_e32 v42, v40, v41
	v_min_u32_e32 v46, v44, v45
	v_max_u32_e32 v40, v40, v41
	v_max_u32_e32 v44, v44, v45
	v_min_u32_e32 v57, v58, v56
	v_min_u32_e32 v29, v59, v28
	v_max_u32_e32 v56, v58, v56
	v_max_u32_e32 v28, v59, v28
	v_min_u32_e32 v53, v54, v52
	v_min_u32_e32 v33, v55, v32
	v_max_u32_e32 v52, v54, v52
	v_max_u32_e32 v32, v55, v32
	v_min_u32_e32 v37, v48, v36
	v_min_u32_e32 v38, v49, v50
	v_max_u32_e32 v36, v48, v36
	v_max_u32_e32 v48, v49, v50
	v_min_u32_e32 v43, v42, v46
	v_max_u32_e32 v42, v42, v46
	v_min_u32_e32 v41, v40, v44
	v_max_u32_e32 v40, v40, v44
	v_min_u32_e32 v31, v57, v29
	v_max_u32_e32 v30, v57, v29
	v_min_u32_e32 v29, v56, v28
	v_max_u32_e32 v28, v56, v28
	v_min_u32_e32 v35, v53, v33
	v_max_u32_e32 v34, v53, v33
	v_min_u32_e32 v33, v52, v32
	v_max_u32_e32 v32, v52, v32
	v_min_u32_e32 v39, v37, v38
	v_max_u32_e32 v38, v37, v38
	v_min_u32_e32 v37, v36, v48
	v_max_u32_e32 v36, v36, v48
	ds_write_b128 v246, v[40:43]
	ds_write_b128 v246, v[36:39] offset:16
	ds_write_b128 v246, v[32:35] offset:32
	ds_write_b128 v246, v[28:31] offset:48
